# P2b: scan items bound statically to 8 WGs per XCD (queue hands out indexer items only); indexer queue atomic no longer waited for before scoring (ticket returned into v186, consumed after the score lo
# speedup vs baseline: 1.0393x; 1.0014x over previous
.LBB0_542:
	s_lshl_b32 s0, s90, 6
	s_ashr_i32 s1, s0, 31
	s_lshl_b64 s[0:1], s[0:1], 2
	s_add_u32 s0, s50, s0
	s_addc_u32 s1, s51, s1
	s_add_u32 s0, s0, 0x20000
	s_addc_u32 s1, s1, 0
	v_writelane_b32 v252, s0, 10
	s_nop 1
	v_writelane_b32 v252, s1, 11
	s_and_saveexec_b64 s[0:1], s[94:95]
	s_cbranch_execz .LBB0_546
	v_readlane_b32 s8, v252, 2
	s_and_b32 s9, s8, 31
	s_cmp_lt_u32 s9, 8
	s_cbranch_scc0 .Lsq_deq
	s_lshr_b32 s8, s8, 5
	s_lshl_b32 s8, s8, 3
	s_add_i32 s8, s8, s9
	v_mov_b32_e32 v1, s8
	s_branch .Lsq_have
.Lsq_deq:
	v_mov_b32_e32 v3, 1
	v_readlane_b32 s8, v252, 10
	v_mov_b32_e32 v2, 0
	v_readlane_b32 s9, v252, 11
	s_nop 4
	global_atomic_add v1, v2, v3, s[8:9] sc0
	s_waitcnt vmcnt(0)
	v_add_u32_e32 v1, 64, v1
.Lsq_have:
	s_add_i32 s4, 0, 0x26d80
	v_mov_b32_e32 v2, s4
	ds_write_b32 v2, v1

.LBB0_562:
	s_waitcnt vmcnt(0)
	s_waitcnt lgkmcnt(0)
	s_barrier
	s_barrier
	s_and_saveexec_b64 s[4:5], s[94:95]
	s_cbranch_execz .LBB0_548
	v_mov_b32_e32 v3, 1
	v_readlane_b32 s12, v252, 10
	v_readlane_b32 s13, v252, 11
	s_nop 4
	global_atomic_add v1, v77, v3, s[12:13] sc0
	s_waitcnt vmcnt(0)
	v_add_u32_e32 v1, 64, v1
	v_mov_b32_e32 v3, s42
	ds_write_b32 v3, v1
	s_branch .LBB0_548

.LBB0_567:
	s_waitcnt vmcnt(0)
	v_mov_b32_e32 v186, 0
	s_and_saveexec_b64 s[0:1], s[94:95]
	s_cbranch_execz .LBB0_571
	v_mov_b32_e32 v3, 1
	v_readlane_b32 s4, v252, 10
	v_readlane_b32 s5, v252, 11
	s_nop 4
	global_atomic_add v186, v179, v3, s[4:5] sc0
.LBB0_571:
	s_or_b64 exec, exec, s[0:1]
	s_sub_i32 s0, s33, 64
	s_ashr_i32 s1, s0, 31
	s_lshr_b32 s1, s1, 29
	s_add_i32 s1, s0, s1
	s_and_b32 s2, s1, -8
	s_sub_i32 s90, s0, s2
	s_ashr_i32 s0, s1, 3
	v_mov_b32_e32 v2, v0
	s_sub_i32 s4, 0x7f, s0
	s_bfe_u32 s6, s4, 0x1b0001
	v_readfirstlane_b32 s0, v2
	s_bfe_u32 s5, s0, 0x30006
	s_cmp_gt_u32 s5, s6
	s_cbranch_scc1 .LBB0_576
	s_ashr_i32 s91, s90, 31
	v_and_b32_e32 v3, 31, v2
	v_bfe_u32 v2, v2, 5, 1
	s_lshl_b64 s[0:1], s[90:91], 11
	v_or_b32_e32 v180, s0, v3
	v_lshlrev_b32_e32 v178, 4, v2
	v_lshlrev_b32_e32 v2, 13, v2
	s_lshl_b32 s0, s5, 7
	v_lshlrev_b32_e32 v3, 2, v3
	v_or3_b32 v2, v2, s0, v3
	v_readlane_b32 s0, v252, 13
	v_lshl_add_u64 v[182:183], s[16:17], 0, v[178:179]
	v_mov_b64_e32 v[176:177], v[132:133]
	v_add_u32_e32 v178, s0, v2
	s_lshl_b32 s0, s5, 5
	v_mov_b64_e32 v[172:173], v[136:137]
	v_mov_b64_e32 v[168:169], v[140:141]
	v_mov_b64_e32 v[164:165], v[144:145]
	v_mov_b64_e32 v[148:149], v[132:133]
	v_mov_b64_e32 v[152:153], v[136:137]
	v_mov_b64_e32 v[156:157], v[140:141]
	v_mov_b64_e32 v[160:161], v[144:145]
	v_lshlrev_b32_e32 v187, 16, v98
	v_and_b32_e32 v188, 0xffff0000, v98
	v_lshlrev_b32_e32 v189, 16, v99
	v_and_b32_e32 v190, 0xffff0000, v99
	v_lshlrev_b32_e32 v191, 16, v100
	v_and_b32_e32 v192, 0xffff0000, v100
	v_lshlrev_b32_e32 v193, 16, v101
	v_and_b32_e32 v194, 0xffff0000, v101
	v_lshlrev_b32_e32 v195, 16, v102
	v_and_b32_e32 v196, 0xffff0000, v102
	v_lshlrev_b32_e32 v197, 16, v103
	v_and_b32_e32 v199, 0xffff0000, v103
	v_lshlrev_b32_e32 v200, 16, v104
	v_and_b32_e32 v201, 0xffff0000, v104
	v_lshlrev_b32_e32 v202, 16, v105
	v_and_b32_e32 v203, 0xffff0000, v105
	v_lshlrev_b32_e32 v204, 16, v106
	v_and_b32_e32 v205, 0xffff0000, v106
	v_lshlrev_b32_e32 v206, 16, v107
	v_and_b32_e32 v207, 0xffff0000, v107
	v_lshlrev_b32_e32 v208, 16, v108
	v_and_b32_e32 v209, 0xffff0000, v108
	v_lshlrev_b32_e32 v210, 16, v109
	v_and_b32_e32 v211, 0xffff0000, v109
	v_lshlrev_b32_e32 v212, 16, v110
	v_and_b32_e32 v213, 0xffff0000, v110
	v_lshlrev_b32_e32 v214, 16, v111
	v_and_b32_e32 v215, 0xffff0000, v111
	v_lshlrev_b32_e32 v216, 16, v112
	v_and_b32_e32 v217, 0xffff0000, v112
	v_lshlrev_b32_e32 v218, 16, v113
	v_and_b32_e32 v219, 0xffff0000, v113
	v_lshlrev_b32_e32 v220, 16, v114
	v_and_b32_e32 v221, 0xffff0000, v114
	v_lshlrev_b32_e32 v222, 16, v115
	v_and_b32_e32 v223, 0xffff0000, v115
	v_lshlrev_b32_e32 v224, 16, v116
	v_and_b32_e32 v225, 0xffff0000, v116
	v_lshlrev_b32_e32 v226, 16, v117
	v_and_b32_e32 v227, 0xffff0000, v117
	v_lshlrev_b32_e32 v228, 16, v118
	v_and_b32_e32 v229, 0xffff0000, v118
	v_lshlrev_b32_e32 v230, 16, v119
	v_and_b32_e32 v231, 0xffff0000, v119
	v_lshlrev_b32_e32 v232, 16, v120
	v_and_b32_e32 v233, 0xffff0000, v120
	v_lshlrev_b32_e32 v234, 16, v121
	v_and_b32_e32 v235, 0xffff0000, v121
	v_lshlrev_b32_e32 v236, 16, v122
	v_and_b32_e32 v237, 0xffff0000, v122
	v_lshlrev_b32_e32 v238, 16, v123
	v_and_b32_e32 v239, 0xffff0000, v123
	v_lshlrev_b32_e32 v240, 16, v124
	v_and_b32_e32 v241, 0xffff0000, v124
	v_lshlrev_b32_e32 v242, 16, v125
	v_and_b32_e32 v243, 0xffff0000, v125
	v_lshlrev_b32_e32 v244, 16, v126
	v_and_b32_e32 v245, 0xffff0000, v126
	v_lshlrev_b32_e32 v246, 16, v127
	v_and_b32_e32 v247, 0xffff0000, v127
	v_lshlrev_b32_e32 v248, 16, v128
	v_and_b32_e32 v249, 0xffff0000, v128
	v_lshlrev_b32_e32 v250, 16, v129
	v_and_b32_e32 v251, 0xffff0000, v129
	v_mov_b32_e32 v181, s1
	s_bitset1_b32 s0, 8
	v_mov_b64_e32 v[174:175], v[130:131]
	v_mov_b64_e32 v[170:171], v[134:135]
	v_mov_b64_e32 v[166:167], v[138:139]
	v_mov_b64_e32 v[162:163], v[142:143]
	v_mov_b64_e32 v[146:147], v[130:131]
	v_mov_b64_e32 v[150:151], v[134:135]
	v_mov_b64_e32 v[154:155], v[138:139]
	v_mov_b64_e32 v[158:159], v[142:143]
	s_branch .LBB0_574

.LBB0_576:
	s_waitcnt lgkmcnt(0)
	s_barrier
	s_and_saveexec_b64 s[0:1], s[94:95]
	v_mov_b32_e32 v2, s97
	s_waitcnt vmcnt(0)
	v_add_u32_e32 v186, 64, v186
	ds_write_b32 v2, v186
	s_or_b64 exec, exec, s[0:1]
	s_waitcnt lgkmcnt(0)
	s_barrier
	v_mov_b32_e32 v2, s97
	ds_read_b32 v2, v2
	s_movk_i32 s0, 0x43f
	s_waitcnt lgkmcnt(0)
	v_cmp_lt_i32_e64 s[18:19], s0, v2
	v_readfirstlane_b32 s33, v2
	s_and_b64 vcc, exec, s[18:19]
	s_cbranch_vccnz .LBB0_580
	s_sub_i32 s0, s33, 64
	s_ashr_i32 s1, s0, 31
	s_lshr_b32 s1, s1, 29
	s_add_i32 s1, s0, s1
	s_and_b32 s2, s1, -8
	s_lshl_b32 s1, s1, 1
	s_sub_i32 s0, s0, s2
	v_mov_b32_e32 v12, v0
	s_and_b32 s1, s1, -16
	s_sub_i32 s3, 0x7f0, s1
	v_readfirstlane_b32 s2, v12
	s_ashr_i32 s1, s0, 31
	s_bfe_u32 s2, s2, 0x30006
	s_lshl_b64 s[0:1], s[0:1], 11
	v_lshrrev_b32_e32 v3, 3, v12
	s_add_u32 s5, s0, s3
	v_bfe_u32 v2, v12, 2, 1
	v_and_b32_e32 v3, 2, v3
	s_addc_u32 s6, s1, 0
	v_and_b32_e32 v4, 3, v12
	v_lshrrev_b32_e32 v5, 1, v12
	v_or3_b32 v2, v2, v3, s5
	v_mov_b32_e32 v3, s6
	v_and_or_b32 v6, v5, 4, v4
	v_lshlrev_b64 v[4:5], 13, v[2:3]
	v_bfe_u32 v13, v12, 5, 1
	v_lshl_add_u64 v[4:5], s[38:39], 0, v[4:5]
	v_lshlrev_b32_e32 v178, 7, v6
	v_lshlrev_b32_e32 v6, 4, v13
	v_mov_b32_e32 v7, v179
	v_lshl_add_u64 v[4:5], v[4:5], 0, v[178:179]
	v_lshl_add_u64 v[4:5], v[4:5], 0, v[6:7]
	s_mov_b64 s[6:7], 0x1600
	v_lshl_add_u64 v[8:9], v[4:5], 0, s[6:7]
	s_movk_i32 s6, 0x1000
	v_add_co_u32_e32 v10, vcc, s6, v4
	s_mov_b64 s[8:9], 0x9600
	s_nop 0
	v_addc_co_u32_e32 v11, vcc, 0, v5, vcc
	s_mov_b32 s7, 0x9000
	global_load_dwordx4 v[34:37], v[8:9], off offset:32
	global_load_dwordx4 v[38:41], v[8:9], off offset:64
	global_load_dwordx4 v[42:45], v[10:11], off offset:1536
	global_load_dwordx4 v[46:49], v[8:9], off offset:96
	v_lshl_add_u64 v[8:9], v[4:5], 0, s[8:9]
	v_add_co_u32_e32 v10, vcc, s7, v4
	s_mov_b64 s[8:9], 0x11600
	s_nop 0
	v_addc_co_u32_e32 v11, vcc, 0, v5, vcc
	global_load_dwordx4 v[50:53], v[8:9], off offset:32
	global_load_dwordx4 v[54:57], v[8:9], off offset:64
	global_load_dwordx4 v[58:61], v[10:11], off offset:1536
	global_load_dwordx4 v[62:65], v[8:9], off offset:96
	v_lshl_add_u64 v[8:9], v[4:5], 0, s[8:9]
	s_mov_b32 s8, 0x11000
	v_add_co_u32_e32 v10, vcc, s8, v4
	s_mov_b64 s[10:11], 0x19600
	s_nop 0
	v_addc_co_u32_e32 v11, vcc, 0, v5, vcc
	s_mov_b32 s9, 0x19000
	v_or_b32_e32 v2, s5, v13
	global_load_dwordx4 v[66:69], v[8:9], off offset:32
	global_load_dwordx4 v[70:73], v[8:9], off offset:64
	global_load_dwordx4 v[74:77], v[10:11], off offset:1536
	global_load_dwordx4 v[78:81], v[8:9], off offset:96
	v_lshl_add_u64 v[8:9], v[4:5], 0, s[10:11]
	v_add_co_u32_e32 v4, vcc, s9, v4
	v_lshlrev_b64 v[2:3], 13, v[2:3]
	s_nop 0
	v_addc_co_u32_e32 v5, vcc, 0, v5, vcc
	v_lshl_add_u64 v[2:3], s[38:39], 0, v[2:3]
	global_load_dwordx4 v[82:85], v[8:9], off offset:32
	global_load_dwordx4 v[86:89], v[8:9], off offset:64
	global_load_dwordx4 v[90:93], v[4:5], off offset:1536
	global_load_dwordx4 v[94:97], v[8:9], off offset:96
	v_add_co_u32_e32 v4, vcc, s6, v2
	s_movk_i32 s5, 0x5000
	s_nop 0
	v_addc_co_u32_e32 v5, vcc, 0, v3, vcc
	v_add_co_u32_e32 v8, vcc, s5, v2
	s_mov_b32 s5, 0xd000
	s_nop 0
	v_addc_co_u32_e32 v9, vcc, 0, v3, vcc
	global_load_dwordx4 v[98:101], v[4:5], off offset:3984
	global_load_dwordx4 v[102:105], v[8:9], off offset:3984
	v_add_co_u32_e32 v4, vcc, s7, v2
	s_lshr_b32 s3, s3, 5
	s_nop 0
	v_addc_co_u32_e32 v5, vcc, 0, v3, vcc
	v_add_co_u32_e32 v8, vcc, s5, v2
	s_mov_b32 s5, 0x15000
	s_nop 0
	v_addc_co_u32_e32 v9, vcc, 0, v3, vcc
	global_load_dwordx4 v[106:109], v[4:5], off offset:3984
	global_load_dwordx4 v[110:113], v[8:9], off offset:3984
	v_add_co_u32_e32 v4, vcc, s8, v2
	s_nop 1
	v_addc_co_u32_e32 v5, vcc, 0, v3, vcc
	v_add_co_u32_e32 v8, vcc, s5, v2
	s_mov_b32 s5, 0x1d000
	s_nop 0
	v_addc_co_u32_e32 v9, vcc, 0, v3, vcc
	global_load_dwordx4 v[114:117], v[4:5], off offset:3984
	global_load_dwordx4 v[118:121], v[8:9], off offset:3984
	v_add_co_u32_e32 v4, vcc, s9, v2
	s_nop 1
	v_addc_co_u32_e32 v5, vcc, 0, v3, vcc
	v_add_co_u32_e32 v2, vcc, s5, v2
	s_lshl_b32 s5, s2, 5
	s_cmp_le_u32 s2, s3
	s_cselect_b32 s2, s5, 0
	v_addc_co_u32_e32 v3, vcc, 0, v3, vcc
	global_load_dwordx4 v[122:125], v[4:5], off offset:3984
	global_load_dwordx4 v[126:129], v[2:3], off offset:3984
	v_and_or_b32 v2, v12, 31, s2
	v_or_b32_e32 v2, s0, v2
	v_mov_b32_e32 v3, s1
	v_lshlrev_b64 v[2:3], 7, v[2:3]
	v_lshl_add_u64 v[2:3], s[16:17], 0, v[2:3]
	v_lshl_add_u64 v[2:3], v[2:3], 0, v[6:7]
	global_load_dwordx4 v[130:133], v[2:3], off
	global_load_dwordx4 v[134:137], v[2:3], off offset:32
	global_load_dwordx4 v[138:141], v[2:3], off offset:64
	global_load_dwordx4 v[142:145], v[2:3], off offset:96
